# final RMSNorm phase: nt hint on the once-read f16 hidden-state row loads
# speedup vs baseline: 1.0037x; 1.0037x over previous
; __device__ __forceinline__ float f16_lo(unsigned u) { return (float)__builtin_bit_cast(h16x2, u)[0]; }
; __device__ __forceinline__ float f16_hi(unsigned u) { return (float)__builtin_bit_cast(h16x2, u)[1]; }
; #define GAS __attribute__((address_space(1)))
; __global__ void __launch_bounds__(NWAVES * 64, 2) mk_fwd(Args args) {
;     ...
;           for (; m < M; m += 2 * NGW) { f32x4 v[2][4]; float ss[2] = {0.f, 0.f};
; #pragma unroll
;               for (int r = 0; r < 2; ++r) { const GAS v2u* xr = (const GAS v2u*)(hx + (size_t)(m + r * NGW) * D) + ln;
; #pragma unroll
;                   for (int q = 0; q < 4; ++q) { const v2u hv = xr[64 * q]; v[r][q] = (f32x4){pg8::f16_lo(hv.x), pg8::f16_hi(hv.x), pg8::f16_lo(hv.y), pg8::f16_hi(hv.y)}; } }
; #pragma unroll
;               for (int r = 0; r < 2; ++r) {
; #pragma unroll
;                   for (int q = 0; q < 4; ++q) ss[r] += (v[r][q].x * v[r][q].x + v[r][q].y * v[r][q].y) + (v[r][q].z * v[r][q].z + v[r][q].w * v[r][q].w);
.LBB0_1358:
	s_ashr_i32 s61, s60, 31
	s_lshl_b64 s[2:3], s[60:61], 11
	s_add_u32 s2, s1, s2
	s_addc_u32 s3, s4, s3
	v_lshl_add_u64 v[16:17], s[2:3], 0, v[4:5]
	global_load_dwordx2 v[20:21], v[16:17], off nt
	global_load_dwordx2 v[22:23], v[16:17], off offset:512 nt
	global_load_dwordx2 v[24:25], v[16:17], off offset:1024 nt
	s_add_i32 s2, s54, s60
	global_load_dwordx2 v[26:27], v[16:17], off offset:1536 nt
	s_ashr_i32 s3, s2, 31
	s_lshl_b64 s[8:9], s[2:3], 11
	s_add_u32 s8, s1, s8
	s_addc_u32 s9, s4, s9
	v_lshl_add_u64 v[28:29], s[8:9], 0, v[4:5]
	global_load_dwordx2 v[30:31], v[28:29], off nt
	global_load_dwordx2 v[32:33], v[28:29], off offset:512 nt
	global_load_dwordx2 v[34:35], v[28:29], off offset:1024 nt
	global_load_dwordx2 v[36:37], v[28:29], off offset:1536 nt
	s_lshl_b64 s[8:9], s[60:61], 12
	s_lshl_b64 s[2:3], s[2:3], 12
	s_add_i32 s60, s60, s5
	s_cmpk_lt_i32 s60, 0x4000
	s_waitcnt vmcnt(0)
	v_cvt_f32_f16_e32 v28, v20
	v_cvt_f32_f16_sdwa v29, v20 dst_sel:DWORD dst_unused:UNUSED_PAD src0_sel:WORD_1
	v_cvt_f32_f16_e32 v20, v21
	v_cvt_f32_f16_sdwa v21, v21 dst_sel:DWORD dst_unused:UNUSED_PAD src0_sel:WORD_1
	v_cvt_f32_f16_e32 v40, v22
	v_cvt_f32_f16_sdwa v41, v22 dst_sel:DWORD dst_unused:UNUSED_PAD src0_sel:WORD_1
	v_cvt_f32_f16_e32 v22, v23
	v_cvt_f32_f16_sdwa v23, v23 dst_sel:DWORD dst_unused:UNUSED_PAD src0_sel:WORD_1
	v_cvt_f32_f16_e32 v42, v24
	v_cvt_f32_f16_sdwa v43, v24 dst_sel:DWORD dst_unused:UNUSED_PAD src0_sel:WORD_1
	v_cvt_f32_f16_e32 v24, v25
	v_cvt_f32_f16_sdwa v25, v25 dst_sel:DWORD dst_unused:UNUSED_PAD src0_sel:WORD_1
	v_cvt_f32_f16_e32 v44, v26
	v_cvt_f32_f16_sdwa v45, v26 dst_sel:DWORD dst_unused:UNUSED_PAD src0_sel:WORD_1
	v_cvt_f32_f16_e32 v26, v27
	v_cvt_f32_f16_sdwa v27, v27 dst_sel:DWORD dst_unused:UNUSED_PAD src0_sel:WORD_1
	v_cvt_f32_f16_e32 v46, v30
	v_cvt_f32_f16_sdwa v47, v30 dst_sel:DWORD dst_unused:UNUSED_PAD src0_sel:WORD_1
	v_cvt_f32_f16_e32 v30, v31
	v_cvt_f32_f16_sdwa v31, v31 dst_sel:DWORD dst_unused:UNUSED_PAD src0_sel:WORD_1
	v_cvt_f32_f16_e32 v48, v32
	v_cvt_f32_f16_sdwa v49, v32 dst_sel:DWORD dst_unused:UNUSED_PAD src0_sel:WORD_1
	v_cvt_f32_f16_e32 v32, v33
	v_cvt_f32_f16_sdwa v33, v33 dst_sel:DWORD dst_unused:UNUSED_PAD src0_sel:WORD_1
	v_mov_b32_e32 v56, v29
	v_mov_b32_e32 v57, v21
	v_mov_b32_e32 v60, v41
	v_mov_b32_e32 v61, v23
	v_mov_b32_e32 v54, v28
	v_mov_b32_e32 v55, v20
	v_mov_b32_e32 v58, v40
	v_mov_b32_e32 v59, v22
	v_mul_f32_e32 v62, v43, v43
	v_mul_f32_e32 v64, v25, v25
	v_pk_mul_f32 v[56:57], v[56:57], v[56:57]
	v_pk_mul_f32 v[60:61], v[60:61], v[60:61]
	v_cvt_f32_f16_e32 v50, v34
	v_cvt_f32_f16_sdwa v51, v34 dst_sel:DWORD dst_unused:UNUSED_PAD src0_sel:WORD_1
	v_cvt_f32_f16_e32 v34, v35
	v_cvt_f32_f16_sdwa v35, v35 dst_sel:DWORD dst_unused:UNUSED_PAD src0_sel:WORD_1
	v_pk_mul_f32 v[68:69], v[26:27], v[26:27]
	v_pk_fma_f32 v[62:63], v[42:43], v[42:43], v[62:63] op_sel_hi:[1,1,0]
	v_pk_fma_f32 v[64:65], v[24:25], v[24:25], v[64:65] op_sel_hi:[1,1,0]
	v_pk_fma_f32 v[54:55], v[54:55], v[54:55], v[56:57]
	v_pk_fma_f32 v[56:57], v[58:59], v[58:59], v[60:61]
	v_cvt_f32_f16_e32 v52, v36
	v_cvt_f32_f16_sdwa v53, v36 dst_sel:DWORD dst_unused:UNUSED_PAD src0_sel:WORD_1
	v_cvt_f32_f16_e32 v36, v37
	v_cvt_f32_f16_sdwa v37, v37 dst_sel:DWORD dst_unused:UNUSED_PAD src0_sel:WORD_1
	v_pk_mul_f32 v[66:67], v[44:45], v[44:45]
	v_mov_b32_e32 v63, v68
	v_mov_b32_e32 v65, v69
	v_pk_add_f32 v[54:55], v[54:55], v[54:55] op_sel:[0,1] op_sel_hi:[1,0]
	v_pk_add_f32 v[56:57], v[56:57], v[56:57] op_sel:[0,1] op_sel_hi:[1,0]
	v_pk_add_f32 v[58:59], v[62:63], v[64:65]
	v_mov_b32_e32 v55, v66
	v_mov_b32_e32 v57, v67
	v_mov_b32_e32 v62, v47
	v_mov_b32_e32 v63, v31
	v_mov_b32_e32 v66, v49
	v_mov_b32_e32 v67, v33
	v_mov_b32_e32 v60, v46
	v_mov_b32_e32 v61, v30
	v_mov_b32_e32 v64, v48
	v_mov_b32_e32 v65, v32
	v_pk_add_f32 v[54:55], v[54:55], v[56:57]
	v_pk_mul_f32 v[56:57], v[62:63], v[62:63]
	v_pk_mul_f32 v[62:63], v[66:67], v[66:67]
	v_mul_f32_e32 v68, v51, v51
	v_mul_f32_e32 v70, v35, v35
	v_pk_add_f32 v[54:55], v[54:55], v[58:59]
	v_pk_fma_f32 v[56:57], v[60:61], v[60:61], v[56:57]
	v_pk_fma_f32 v[58:59], v[64:65], v[64:65], v[62:63]
	v_pk_fma_f32 v[66:67], v[50:51], v[50:51], v[68:69] op_sel_hi:[1,1,0]
	v_pk_add_f32 v[56:57], v[56:57], v[56:57] op_sel:[0,1] op_sel_hi:[1,0]
	v_pk_add_f32 v[58:59], v[58:59], v[58:59] op_sel:[0,1] op_sel_hi:[1,0]
	v_pk_fma_f32 v[60:61], v[34:35], v[34:35], v[70:71] op_sel_hi:[1,1,0]
	v_pk_mul_f32 v[62:63], v[52:53], v[52:53]
	v_pk_mul_f32 v[64:65], v[36:37], v[36:37]
	v_mov_b32_e32 v57, v62
	v_mov_b32_e32 v59, v63
	v_mov_b32_e32 v67, v64
	v_mov_b32_e32 v61, v65
	v_pk_add_f32 v[56:57], v[56:57], v[58:59]
	v_pk_add_f32 v[58:59], v[66:67], v[60:61]
	s_waitcnt lgkmcnt(0)
; #define GAS __attribute__((address_space(1)))
; __device__ __forceinline__ float wave_sum(float v, int lane) {
; #pragma unroll
;     for (int o = 1; o < 64; o <<= 1) v += __builtin_bit_cast(float, __builtin_amdgcn_ds_bpermute((lane ^ o) << 2, __builtin_bit_cast(int, v)));
;     return v;
; __global__ void __launch_bounds__(NWAVES * 64, 2) mk_fwd(Args args) {
;     ...
;               for (int r = 0; r < 2; ++r) {
; #pragma unroll
;                   for (int q = 0; q < 4; ++q) ss[r] += (v[r][q].x * v[r][q].x + v[r][q].y * v[r][q].y) + (v[r][q].z * v[r][q].z + v[r][q].w * v[r][q].w);
;                   const float rstd = rsqrtf(wave_sum(ss[r], ln) * (1.f / D) + EPS); GAS f32x4* o = (GAS f32x4*)(ap->out + (size_t)(m + r * NGW) * D) + ln;
; #pragma unroll
;                   for (int q = 0; q < 4; ++q) o[64 * q] = v[r][q] * rstd * gr[64 * q]; } } }
	v_lshl_add_u64 v[38:39], v[88:89], 0, s[8:9]
	v_pk_add_f32 v[56:57], v[56:57], v[58:59]
	v_mov_b32_e32 v59, v54
	v_mov_b32_e32 v58, v56
	v_mov_b32_e32 v54, v57
	v_pk_add_f32 v[54:55], v[58:59], v[54:55]
	ds_bpermute_b32 v57, v3, v55
	ds_bpermute_b32 v56, v3, v54
	s_waitcnt lgkmcnt(0)
	v_pk_add_f32 v[54:55], v[54:55], v[56:57]
	ds_bpermute_b32 v57, v10, v55
	ds_bpermute_b32 v56, v10, v54
	s_waitcnt lgkmcnt(0)
	v_pk_add_f32 v[54:55], v[54:55], v[56:57]
	ds_bpermute_b32 v57, v11, v55
	ds_bpermute_b32 v56, v11, v54
	s_waitcnt lgkmcnt(0)
	v_pk_add_f32 v[54:55], v[54:55], v[56:57]
	ds_bpermute_b32 v57, v12, v55
	ds_bpermute_b32 v56, v12, v54
	s_waitcnt lgkmcnt(0)
	v_pk_add_f32 v[54:55], v[54:55], v[56:57]
	ds_bpermute_b32 v57, v13, v55
	ds_bpermute_b32 v56, v13, v54
	s_waitcnt lgkmcnt(0)
	v_pk_add_f32 v[54:55], v[54:55], v[56:57]
	ds_bpermute_b32 v57, v14, v55
	ds_bpermute_b32 v56, v14, v54
	s_waitcnt lgkmcnt(0)
	v_pk_add_f32 v[54:55], v[54:55], v[56:57]
	s_nop 0
	v_pk_fma_f32 v[54:55], v[54:55], s[0:1], v[2:3] op_sel_hi:[1,0,0]
	s_nop 0
	v_mul_f32_e32 v15, 0x4b800000, v55
	v_cmp_gt_f32_e32 vcc, s6, v55
	s_nop 1
	v_cndmask_b32_e32 v15, v55, v15, vcc
	v_rsq_f32_e32 v15, v15
	s_nop 0
	v_mul_f32_e32 v55, 0x45800000, v15
	v_cndmask_b32_e32 v56, v15, v55, vcc
	v_pk_mul_f32 v[28:29], v[56:57], v[28:29] op_sel_hi:[0,1]
	v_pk_mul_f32 v[20:21], v[56:57], v[20:21] op_sel_hi:[0,1]
	v_pk_mul_f32 v[18:19], v[20:21], v[74:75]
	v_pk_mul_f32 v[16:17], v[28:29], v[72:73]
	global_store_dwordx4 v[38:39], v[16:19], off sc1
	v_pk_mul_f32 v[20:21], v[56:57], v[22:23] op_sel_hi:[0,1]
	v_pk_mul_f32 v[22:23], v[56:57], v[40:41] op_sel_hi:[0,1]
	v_mul_f32_e32 v15, 0x4b800000, v54
	v_cmp_gt_f32_e32 vcc, s6, v54
	v_pk_mul_f32 v[90:91], v[22:23], v[76:77]
	v_pk_mul_f32 v[92:93], v[20:21], v[78:79]
	global_store_dwordx4 v[38:39], v[90:93], off offset:1024 sc1
	v_pk_mul_f32 v[20:21], v[56:57], v[24:25] op_sel_hi:[0,1]
	v_pk_mul_f32 v[22:23], v[56:57], v[42:43] op_sel_hi:[0,1]
	v_cndmask_b32_e32 v15, v54, v15, vcc
	v_rsq_f32_e32 v15, v15
	v_pk_mul_f32 v[94:95], v[22:23], v[80:81]
	v_pk_mul_f32 v[96:97], v[20:21], v[82:83]
	global_store_dwordx4 v[38:39], v[94:97], off offset:2048 sc1
	v_pk_mul_f32 v[20:21], v[56:57], v[26:27] op_sel_hi:[0,1]
	v_pk_mul_f32 v[22:23], v[56:57], v[44:45] op_sel_hi:[0,1]
	v_pk_mul_f32 v[98:99], v[22:23], v[84:85]
	v_pk_mul_f32 v[100:101], v[20:21], v[86:87]
	global_store_dwordx4 v[38:39], v[98:101], off offset:3072 sc1
	v_mul_f32_e32 v22, 0x45800000, v15
	v_cndmask_b32_e32 v22, v15, v22, vcc
	v_pk_mul_f32 v[24:25], v[22:23], v[30:31] op_sel_hi:[0,1]
	v_pk_mul_f32 v[26:27], v[22:23], v[46:47] op_sel_hi:[0,1]
	v_lshl_add_u64 v[20:21], v[88:89], 0, s[2:3]
	v_pk_mul_f32 v[102:103], v[26:27], v[72:73]
	v_pk_mul_f32 v[104:105], v[24:25], v[74:75]
	global_store_dwordx4 v[20:21], v[102:105], off sc1
	v_pk_mul_f32 v[24:25], v[22:23], v[32:33] op_sel_hi:[0,1]
	v_pk_mul_f32 v[26:27], v[22:23], v[48:49] op_sel_hi:[0,1]
	v_pk_mul_f32 v[106:107], v[26:27], v[76:77]
	v_pk_mul_f32 v[108:109], v[24:25], v[78:79]
	global_store_dwordx4 v[20:21], v[106:109], off offset:1024 sc1
	v_pk_mul_f32 v[24:25], v[22:23], v[34:35] op_sel_hi:[0,1]
	v_pk_mul_f32 v[26:27], v[22:23], v[50:51] op_sel_hi:[0,1]
	v_pk_mul_f32 v[110:111], v[26:27], v[80:81]
	v_pk_mul_f32 v[112:113], v[24:25], v[82:83]
	global_store_dwordx4 v[20:21], v[110:113], off offset:2048 sc1
	v_pk_mul_f32 v[24:25], v[22:23], v[36:37] op_sel_hi:[0,1]
	v_pk_mul_f32 v[22:23], v[22:23], v[52:53] op_sel_hi:[0,1]
	v_pk_mul_f32 v[114:115], v[22:23], v[84:85]
	v_pk_mul_f32 v[116:117], v[24:25], v[86:87]
	global_store_dwordx4 v[20:21], v[114:117], off offset:3072 sc1
	s_cbranch_scc1 .LBB0_1358
